# v35 + differential attention: s_setprio 1 from the QK fragment chain to the end of the P.V ring (softmax of the partner wave yields), s_setprio 0 after
# baseline (speedup 1.0000x reference)
.LBB0_833:
	s_add_i32 s30, s72, -1
	s_cmp_ge_u32 s30, s90
	s_cbranch_scc1 .LBB0_846
	s_cmp_lt_u32 s72, s90
	v_cmp_eq_f32_e64 s[30:31], s1, v173
	s_cselect_b64 s[52:53], -1, 0
	s_cmp_ge_u32 s72, s90
	v_cndmask_b32_e64 v185, v173, 0, s[30:31]
	s_cbranch_scc1 .LBB0_836
	s_mul_i32 s34, s71, 0x6000
	v_add_u32_e32 v147, s34, v169
	ds_read_b128 v[148:151], v147
	v_xor_b32_e32 v98, 0x80000000, v185
	v_mov_b32_e32 v99, v98
	v_mov_b32_e32 v100, v98
	v_mov_b32_e32 v101, v98
	v_mov_b32_e32 v102, v98
	v_mov_b32_e32 v103, v98
	v_mov_b32_e32 v104, v98
	v_mov_b32_e32 v105, v98
	v_mov_b32_e32 v106, v98
	v_mov_b32_e32 v107, v98
	v_mov_b32_e32 v108, v98
	v_mov_b32_e32 v109, v98
	v_mov_b32_e32 v110, v98
	v_mov_b32_e32 v111, v98
	v_mov_b32_e32 v112, v98
	v_mov_b32_e32 v113, v98
	ds_read_b128 v[152:155], v147 offset:4096
	v_add_u32_e32 v147, s34, v170
	ds_read_b128 v[156:159], v147
	ds_read_b128 v[188:191], v147 offset:4096
	v_add_u32_e32 v147, s34, v171
	ds_read_b128 v[192:195], v147
	ds_read_b128 v[196:199], v147 offset:4096
	v_add_u32_e32 v147, s34, v172
	ds_read_b128 v[208:211], v147
	ds_read_b128 v[212:215], v147 offset:4096
	s_setprio 1
	s_waitcnt lgkmcnt(7)
	s_nop 0
	v_mfma_f32_32x32x16_f16 v[114:129], v[148:151], v[130:133], v[98:113]
	s_waitcnt lgkmcnt(6)
	v_mfma_f32_32x32x16_f16 v[98:113], v[152:155], v[130:133], v[98:113]
	s_waitcnt lgkmcnt(5)
	v_mfma_f32_32x32x16_f16 v[114:129], v[156:159], v[134:137], v[114:129]
	s_waitcnt lgkmcnt(4)
	v_mfma_f32_32x32x16_f16 v[98:113], v[188:191], v[134:137], v[98:113]
	s_waitcnt lgkmcnt(3)
	v_mfma_f32_32x32x16_f16 v[114:129], v[192:195], v[138:141], v[114:129]
	s_waitcnt lgkmcnt(2)
	v_mfma_f32_32x32x16_f16 v[98:113], v[196:199], v[138:141], v[98:113]
	s_waitcnt lgkmcnt(1)
	v_mfma_f32_32x32x16_f16 v[114:129], v[208:211], v[142:145], v[114:129]
	s_waitcnt lgkmcnt(0)
	v_mfma_f32_32x32x16_f16 v[98:113], v[212:215], v[142:145], v[98:113]

.LBB0_842:
	v_exp_f32_e32 v2, v2
	v_exp_f32_e32 v3, v3
	v_exp_f32_e32 v4, v4
	v_exp_f32_e32 v5, v5
	v_exp_f32_e32 v6, v6
	v_exp_f32_e32 v7, v7
	v_exp_f32_e32 v18, v18
	v_exp_f32_e32 v19, v19
	v_exp_f32_e32 v8, v8
	v_exp_f32_e32 v9, v9
	v_exp_f32_e32 v20, v20
	v_exp_f32_e32 v21, v21
	v_pk_add_f32 v[208:209], v[2:3], 0 op_sel_hi:[1,0]
	v_exp_f32_e32 v10, v10
	v_exp_f32_e32 v11, v11
	v_pk_add_f32 v[208:209], v[4:5], v[208:209]
	v_exp_f32_e32 v22, v22
	v_exp_f32_e32 v23, v23
	v_exp_f32_e32 v24, v24
	v_exp_f32_e32 v25, v25
	v_exp_f32_e32 v12, v12
	v_exp_f32_e32 v13, v13
	v_pk_add_f32 v[208:209], v[6:7], v[208:209]
	v_pk_add_f32 v[196:197], v[18:19], 0 op_sel_hi:[1,0]
	v_pk_add_f32 v[208:209], v[8:9], v[208:209]
	v_exp_f32_e32 v26, v26
	v_exp_f32_e32 v27, v27
	v_pk_add_f32 v[196:197], v[20:21], v[196:197]
	v_exp_f32_e32 v28, v28
	v_exp_f32_e32 v29, v29
	v_pk_add_f32 v[208:209], v[10:11], v[208:209]
	v_pk_add_f32 v[196:197], v[22:23], v[196:197]
	v_pk_add_f32 v[212:213], v[12:13], v[208:209]
	v_exp_f32_e32 v30, v30
	v_exp_f32_e32 v31, v31
	v_exp_f32_e32 v14, v14
	v_exp_f32_e32 v15, v15
	v_cvt_pk_f16_f32 v208, v18, v19
	v_cvt_pk_f16_f32 v209, v20, v21
	v_cvt_pk_f16_f32 v210, v22, v23
	v_cvt_pk_f16_f32 v211, v24, v25
	v_pk_add_f32 v[196:197], v[24:25], v[196:197]
	v_exp_f32_e32 v32, v32
	v_exp_f32_e32 v33, v33
	s_waitcnt lgkmcnt(0)
	v_mfma_f32_32x32x16_f16 v[82:97], v[158:161], v[208:211], v[82:97]
	v_exp_f32_e32 v16, v16
	v_exp_f32_e32 v17, v17
	v_pk_add_f32 v[196:197], v[26:27], v[196:197]
	v_pk_add_f32 v[160:161], v[14:15], v[212:213]
	v_pk_add_f32 v[196:197], v[28:29], v[196:197]
	v_pk_add_f32 v[160:161], v[16:17], v[160:161]
	v_pk_add_f32 v[158:159], v[30:31], v[196:197]
	v_mfma_f32_32x32x16_f16 v[66:81], v[154:157], v[208:211], v[66:81]
	v_add_f32_e64 v158, v32, v158
	v_add_f32_e64 v159, v33, v159
	v_cvt_pk_f16_f32 v154, v26, v27
	v_add_f32_e64 v158, v160, v158
	v_add_f32_e64 v159, v161, v159
	v_cvt_pk_f16_f32 v155, v28, v29
	v_add_f32_e32 v195, v158, v159
	v_add_f32_e32 v184, v184, v195
	v_cvt_pk_f16_f32 v156, v30, v31
	v_mfma_f32_32x32x16_f16 v[50:65], v[150:153], v[208:211], v[50:65]
	v_cvt_pk_f16_f32 v157, v32, v33
	v_cvt_pk_f16_f32 v158, v2, v3
	v_cvt_pk_f16_f32 v159, v4, v5
	v_cvt_pk_f16_f32 v160, v6, v7
	v_cvt_pk_f16_f32 v161, v8, v9
	v_cvt_pk_f16_f32 v150, v10, v11
	v_cvt_pk_f16_f32 v151, v12, v13
	v_mfma_f32_32x32x16_f16 v[34:49], v[146:149], v[208:211], v[34:49]
	v_cvt_pk_f16_f32 v152, v14, v15
	v_cvt_pk_f16_f32 v153, v16, v17
	s_and_b64 vcc, exec, s[34:35]
	ds_read_b64_tr_b16 v[146:147], v192 offset:12288
	ds_read_b64_tr_b16 v[148:149], v193 offset:12288
	ds_read_b64_tr_b16 v[196:197], v191 offset:12288
	ds_read_b64_tr_b16 v[198:199], v186 offset:12288
	ds_read_b64_tr_b16 v[212:213], v189 offset:12288
	ds_read_b64_tr_b16 v[214:215], v187 offset:12288
	ds_read_b64_tr_b16 v[216:217], v190 offset:12288
	ds_read_b64_tr_b16 v[218:219], v188 offset:12288
	ds_read_b64_tr_b16 v[220:221], v192 offset:16384
	ds_read_b64_tr_b16 v[222:223], v193 offset:16384
	s_waitcnt lgkmcnt(8)
	v_mfma_f32_32x32x16_f16 v[82:97], v[146:149], v[154:157], v[82:97]
	ds_read_b64_tr_b16 v[224:225], v191 offset:16384
	ds_read_b64_tr_b16 v[226:227], v186 offset:16384
	s_waitcnt lgkmcnt(8)
	v_mfma_f32_32x32x16_f16 v[66:81], v[196:199], v[154:157], v[66:81]
	ds_read_b64_tr_b16 v[146:147], v189 offset:16384
	ds_read_b64_tr_b16 v[148:149], v187 offset:16384
	s_waitcnt lgkmcnt(8)
	v_mfma_f32_32x32x16_f16 v[50:65], v[212:215], v[154:157], v[50:65]
	ds_read_b64_tr_b16 v[196:197], v190 offset:16384
	ds_read_b64_tr_b16 v[198:199], v188 offset:16384
	s_waitcnt lgkmcnt(8)
	v_mfma_f32_32x32x16_f16 v[34:49], v[216:219], v[154:157], v[34:49]
	ds_read_b64_tr_b16 v[212:213], v192 offset:20480
	ds_read_b64_tr_b16 v[214:215], v193 offset:20480
	s_waitcnt lgkmcnt(8)
	v_mfma_f32_32x32x16_f16 v[82:97], v[220:223], v[158:161], v[82:97]
	ds_read_b64_tr_b16 v[216:217], v191 offset:20480
	ds_read_b64_tr_b16 v[218:219], v186 offset:20480
	s_waitcnt lgkmcnt(8)
	v_mfma_f32_32x32x16_f16 v[66:81], v[224:227], v[158:161], v[66:81]
	ds_read_b64_tr_b16 v[220:221], v189 offset:20480
	ds_read_b64_tr_b16 v[222:223], v187 offset:20480
	s_waitcnt lgkmcnt(8)
	v_mfma_f32_32x32x16_f16 v[50:65], v[146:149], v[158:161], v[50:65]
	ds_read_b64_tr_b16 v[224:225], v190 offset:20480
	ds_read_b64_tr_b16 v[226:227], v188 offset:20480
	s_waitcnt lgkmcnt(8)
	v_mfma_f32_32x32x16_f16 v[34:49], v[196:199], v[158:161], v[34:49]
	s_waitcnt lgkmcnt(6)
	v_mfma_f32_32x32x16_f16 v[82:97], v[212:215], v[150:153], v[82:97]
	s_waitcnt lgkmcnt(4)
	v_mfma_f32_32x32x16_f16 v[66:81], v[216:219], v[150:153], v[66:81]
	s_waitcnt lgkmcnt(2)
	v_mfma_f32_32x32x16_f16 v[50:65], v[220:223], v[150:153], v[50:65]
	s_waitcnt lgkmcnt(0)
	v_mfma_f32_32x32x16_f16 v[34:49], v[224:227], v[150:153], v[34:49]
	s_setprio 0
	v_mov_b32_e32 v146, 0
	s_cbranch_vccnz .LBB0_846
	s_mov_b32 s29, 0x41000000
	v_cmp_lg_f32_e64 s[34:35], s1, v194
	v_cmp_lt_f32_e32 vcc, s29, v194
	s_and_b64 s[30:31], s[30:31], s[34:35]
	s_or_b64 s[30:31], vcc, s[30:31]
	v_cndmask_b32_e64 v146, 0, 1, s[30:31]
	v_cmp_ne_u32_e32 vcc, 0, v146
	s_cbranch_vccz .LBB0_845
	v_add_f32_e32 v146, v185, v194
	v_max_f32_e32 v147, v173, v173
	v_max_f32_e32 v173, v147, v146
	v_cmp_neq_f32_e32 vcc, s1, v173
	s_nop 1
	v_cndmask_b32_e32 v146, 0, v173, vcc
	v_sub_f32_e32 v146, v146, v185
	v_exp_f32_e64 v148, -v146
	s_nop 0
	v_pk_mul_f32 v[96:97], v[148:149], v[96:97] op_sel_hi:[0,1]
	v_pk_mul_f32 v[94:95], v[148:149], v[94:95] op_sel_hi:[0,1]
	v_pk_mul_f32 v[92:93], v[148:149], v[92:93] op_sel_hi:[0,1]
	v_pk_mul_f32 v[90:91], v[148:149], v[90:91] op_sel_hi:[0,1]
	v_pk_mul_f32 v[88:89], v[148:149], v[88:89] op_sel_hi:[0,1]
	v_pk_mul_f32 v[86:87], v[148:149], v[86:87] op_sel_hi:[0,1]
	v_pk_mul_f32 v[84:85], v[148:149], v[84:85] op_sel_hi:[0,1]
	v_pk_mul_f32 v[82:83], v[148:149], v[82:83] op_sel_hi:[0,1]
	v_pk_mul_f32 v[80:81], v[148:149], v[80:81] op_sel_hi:[0,1]
	v_pk_mul_f32 v[78:79], v[148:149], v[78:79] op_sel_hi:[0,1]
	v_pk_mul_f32 v[76:77], v[148:149], v[76:77] op_sel_hi:[0,1]
	v_pk_mul_f32 v[74:75], v[148:149], v[74:75] op_sel_hi:[0,1]
	v_pk_mul_f32 v[72:73], v[148:149], v[72:73] op_sel_hi:[0,1]
	v_pk_mul_f32 v[70:71], v[148:149], v[70:71] op_sel_hi:[0,1]
	v_pk_mul_f32 v[68:69], v[148:149], v[68:69] op_sel_hi:[0,1]
	v_pk_mul_f32 v[66:67], v[148:149], v[66:67] op_sel_hi:[0,1]
	v_pk_mul_f32 v[64:65], v[148:149], v[64:65] op_sel_hi:[0,1]
	v_pk_mul_f32 v[62:63], v[148:149], v[62:63] op_sel_hi:[0,1]
	v_pk_mul_f32 v[60:61], v[148:149], v[60:61] op_sel_hi:[0,1]
	v_pk_mul_f32 v[58:59], v[148:149], v[58:59] op_sel_hi:[0,1]
	v_pk_mul_f32 v[56:57], v[148:149], v[56:57] op_sel_hi:[0,1]
	v_pk_mul_f32 v[54:55], v[148:149], v[54:55] op_sel_hi:[0,1]
	v_pk_mul_f32 v[52:53], v[148:149], v[52:53] op_sel_hi:[0,1]
	v_pk_mul_f32 v[50:51], v[148:149], v[50:51] op_sel_hi:[0,1]
	v_pk_mul_f32 v[48:49], v[148:149], v[48:49] op_sel_hi:[0,1]
	v_pk_mul_f32 v[46:47], v[148:149], v[46:47] op_sel_hi:[0,1]
	v_pk_mul_f32 v[44:45], v[148:149], v[44:45] op_sel_hi:[0,1]
	v_pk_mul_f32 v[42:43], v[148:149], v[42:43] op_sel_hi:[0,1]
	v_pk_mul_f32 v[40:41], v[148:149], v[40:41] op_sel_hi:[0,1]
	v_pk_mul_f32 v[38:39], v[148:149], v[38:39] op_sel_hi:[0,1]
	v_pk_mul_f32 v[36:37], v[148:149], v[36:37] op_sel_hi:[0,1]
	v_pk_mul_f32 v[34:35], v[148:149], v[34:35] op_sel_hi:[0,1]
	v_mul_f32_e32 v184, v184, v148
	s_branch .LBB0_846

.LBB0_851:
	s_cmp_ge_u32 s72, s90
	s_cbranch_scc1 .LBB0_865
	s_cmp_lt_u32 s74, s90
	v_cmp_eq_f32_e64 s[30:31], s1, v173
	s_cselect_b64 s[52:53], -1, 0
	s_cmp_ge_u32 s74, s90
	v_cndmask_b32_e64 v185, v173, 0, s[30:31]
	s_cbranch_scc1 .LBB0_854
	s_mul_i32 s34, s75, 0x6000
	v_add_u32_e32 v147, s34, v169
	ds_read_b128 v[148:151], v147
	v_xor_b32_e32 v2, 0x80000000, v185
	v_mov_b32_e32 v3, v2
	v_mov_b32_e32 v4, v2
	v_mov_b32_e32 v5, v2
	v_mov_b32_e32 v6, v2
	v_mov_b32_e32 v7, v2
	v_mov_b32_e32 v8, v2
	v_mov_b32_e32 v9, v2
	v_mov_b32_e32 v10, v2
	v_mov_b32_e32 v11, v2
	v_mov_b32_e32 v12, v2
	v_mov_b32_e32 v13, v2
	v_mov_b32_e32 v14, v2
	v_mov_b32_e32 v15, v2
	v_mov_b32_e32 v16, v2
	v_mov_b32_e32 v17, v2
	ds_read_b128 v[152:155], v147 offset:4096
	v_add_u32_e32 v147, s34, v170
	ds_read_b128 v[156:159], v147
	ds_read_b128 v[188:191], v147 offset:4096
	v_add_u32_e32 v147, s34, v171
	ds_read_b128 v[192:195], v147
	ds_read_b128 v[196:199], v147 offset:4096
	v_add_u32_e32 v147, s34, v172
	ds_read_b128 v[208:211], v147
	ds_read_b128 v[212:215], v147 offset:4096
	s_setprio 1
	s_waitcnt lgkmcnt(7)
	s_nop 0
	v_mfma_f32_32x32x16_f16 v[18:33], v[148:151], v[130:133], v[2:17]
	s_waitcnt lgkmcnt(6)
	v_mfma_f32_32x32x16_f16 v[2:17], v[152:155], v[130:133], v[2:17]
	s_waitcnt lgkmcnt(5)
	v_mfma_f32_32x32x16_f16 v[18:33], v[156:159], v[134:137], v[18:33]
	s_waitcnt lgkmcnt(4)
	v_mfma_f32_32x32x16_f16 v[2:17], v[188:191], v[134:137], v[2:17]
	s_waitcnt lgkmcnt(3)
	v_mfma_f32_32x32x16_f16 v[18:33], v[192:195], v[138:141], v[18:33]
	s_waitcnt lgkmcnt(2)
	v_mfma_f32_32x32x16_f16 v[2:17], v[196:199], v[138:141], v[2:17]
	s_waitcnt lgkmcnt(1)
	v_mfma_f32_32x32x16_f16 v[18:33], v[208:211], v[142:145], v[18:33]
	s_waitcnt lgkmcnt(0)
	v_mfma_f32_32x32x16_f16 v[2:17], v[212:215], v[142:145], v[2:17]

.LBB0_860:
	v_exp_f32_e32 v98, v98
	v_exp_f32_e32 v99, v99
	v_exp_f32_e32 v100, v100
	v_exp_f32_e32 v101, v101
	v_exp_f32_e32 v102, v102
	v_exp_f32_e32 v103, v103
	v_exp_f32_e32 v114, v114
	v_exp_f32_e32 v115, v115
	v_exp_f32_e32 v104, v104
	v_exp_f32_e32 v105, v105
	v_exp_f32_e32 v116, v116
	v_exp_f32_e32 v117, v117
	v_pk_add_f32 v[208:209], v[98:99], 0 op_sel_hi:[1,0]
	v_exp_f32_e32 v106, v106
	v_exp_f32_e32 v107, v107
	v_pk_add_f32 v[208:209], v[100:101], v[208:209]
	v_exp_f32_e32 v118, v118
	v_exp_f32_e32 v119, v119
	v_exp_f32_e32 v120, v120
	v_exp_f32_e32 v121, v121
	v_exp_f32_e32 v108, v108
	v_exp_f32_e32 v109, v109
	v_pk_add_f32 v[208:209], v[102:103], v[208:209]
	v_pk_add_f32 v[196:197], v[114:115], 0 op_sel_hi:[1,0]
	v_pk_add_f32 v[208:209], v[104:105], v[208:209]
	v_exp_f32_e32 v122, v122
	v_exp_f32_e32 v123, v123
	v_pk_add_f32 v[196:197], v[116:117], v[196:197]
	v_exp_f32_e32 v124, v124
	v_exp_f32_e32 v125, v125
	v_pk_add_f32 v[208:209], v[106:107], v[208:209]
	v_pk_add_f32 v[196:197], v[118:119], v[196:197]
	v_pk_add_f32 v[212:213], v[108:109], v[208:209]
	v_exp_f32_e32 v126, v126
	v_exp_f32_e32 v127, v127
	v_exp_f32_e32 v110, v110
	v_exp_f32_e32 v111, v111
	v_cvt_pk_f16_f32 v208, v114, v115
	v_cvt_pk_f16_f32 v209, v116, v117
	v_cvt_pk_f16_f32 v210, v118, v119
	v_cvt_pk_f16_f32 v211, v120, v121
	v_pk_add_f32 v[196:197], v[120:121], v[196:197]
	v_exp_f32_e32 v128, v128
	v_exp_f32_e32 v129, v129
	s_waitcnt lgkmcnt(0)
	v_mfma_f32_32x32x16_f16 v[82:97], v[158:161], v[208:211], v[82:97]
	v_exp_f32_e32 v112, v112
	v_exp_f32_e32 v113, v113
	v_pk_add_f32 v[196:197], v[122:123], v[196:197]
	v_pk_add_f32 v[160:161], v[110:111], v[212:213]
	v_pk_add_f32 v[196:197], v[124:125], v[196:197]
	v_pk_add_f32 v[160:161], v[112:113], v[160:161]
	v_pk_add_f32 v[158:159], v[126:127], v[196:197]
	v_mfma_f32_32x32x16_f16 v[66:81], v[154:157], v[208:211], v[66:81]
	v_add_f32_e64 v158, v128, v158
	v_add_f32_e64 v159, v129, v159
	v_cvt_pk_f16_f32 v154, v122, v123
	v_add_f32_e64 v158, v158, v160
	v_add_f32_e64 v159, v159, v161
	v_cvt_pk_f16_f32 v155, v124, v125
	v_add_f32_e32 v195, v158, v159
	v_add_f32_e32 v184, v184, v195
	v_cvt_pk_f16_f32 v156, v126, v127
	v_mfma_f32_32x32x16_f16 v[50:65], v[150:153], v[208:211], v[50:65]
	v_cvt_pk_f16_f32 v157, v128, v129
	v_cvt_pk_f16_f32 v158, v98, v99
	v_cvt_pk_f16_f32 v159, v100, v101
	v_cvt_pk_f16_f32 v160, v102, v103
	v_cvt_pk_f16_f32 v161, v104, v105
	v_cvt_pk_f16_f32 v150, v106, v107
	v_cvt_pk_f16_f32 v151, v108, v109
	v_mfma_f32_32x32x16_f16 v[34:49], v[146:149], v[208:211], v[34:49]
	v_cvt_pk_f16_f32 v152, v110, v111
	v_cvt_pk_f16_f32 v153, v112, v113
	s_and_b64 vcc, exec, s[34:35]
	ds_read_b64_tr_b16 v[146:147], v192 offset:12288
	ds_read_b64_tr_b16 v[148:149], v193 offset:12288
	ds_read_b64_tr_b16 v[196:197], v191 offset:12288
	ds_read_b64_tr_b16 v[198:199], v186 offset:12288
	ds_read_b64_tr_b16 v[212:213], v189 offset:12288
	ds_read_b64_tr_b16 v[214:215], v187 offset:12288
	ds_read_b64_tr_b16 v[216:217], v190 offset:12288
	ds_read_b64_tr_b16 v[218:219], v188 offset:12288
	ds_read_b64_tr_b16 v[220:221], v192 offset:16384
	ds_read_b64_tr_b16 v[222:223], v193 offset:16384
	s_waitcnt lgkmcnt(8)
	v_mfma_f32_32x32x16_f16 v[82:97], v[146:149], v[154:157], v[82:97]
	ds_read_b64_tr_b16 v[224:225], v191 offset:16384
	ds_read_b64_tr_b16 v[226:227], v186 offset:16384
	s_waitcnt lgkmcnt(8)
	v_mfma_f32_32x32x16_f16 v[66:81], v[196:199], v[154:157], v[66:81]
	ds_read_b64_tr_b16 v[146:147], v189 offset:16384
	ds_read_b64_tr_b16 v[148:149], v187 offset:16384
	s_waitcnt lgkmcnt(8)
	v_mfma_f32_32x32x16_f16 v[50:65], v[212:215], v[154:157], v[50:65]
	ds_read_b64_tr_b16 v[196:197], v190 offset:16384
	ds_read_b64_tr_b16 v[198:199], v188 offset:16384
	s_waitcnt lgkmcnt(8)
	v_mfma_f32_32x32x16_f16 v[34:49], v[216:219], v[154:157], v[34:49]
	ds_read_b64_tr_b16 v[212:213], v192 offset:20480
	ds_read_b64_tr_b16 v[214:215], v193 offset:20480
	s_waitcnt lgkmcnt(8)
	v_mfma_f32_32x32x16_f16 v[82:97], v[220:223], v[158:161], v[82:97]
	ds_read_b64_tr_b16 v[216:217], v191 offset:20480
	ds_read_b64_tr_b16 v[218:219], v186 offset:20480
	s_waitcnt lgkmcnt(8)
	v_mfma_f32_32x32x16_f16 v[66:81], v[224:227], v[158:161], v[66:81]
	ds_read_b64_tr_b16 v[220:221], v189 offset:20480
	ds_read_b64_tr_b16 v[222:223], v187 offset:20480
	s_waitcnt lgkmcnt(8)
	v_mfma_f32_32x32x16_f16 v[50:65], v[146:149], v[158:161], v[50:65]
	ds_read_b64_tr_b16 v[224:225], v190 offset:20480
	ds_read_b64_tr_b16 v[226:227], v188 offset:20480
	s_waitcnt lgkmcnt(8)
	v_mfma_f32_32x32x16_f16 v[34:49], v[196:199], v[158:161], v[34:49]
	s_waitcnt lgkmcnt(6)
	v_mfma_f32_32x32x16_f16 v[82:97], v[212:215], v[150:153], v[82:97]
	s_waitcnt lgkmcnt(4)
	v_mfma_f32_32x32x16_f16 v[66:81], v[216:219], v[150:153], v[66:81]
	s_waitcnt lgkmcnt(2)
	v_mfma_f32_32x32x16_f16 v[50:65], v[220:223], v[150:153], v[50:65]
	s_waitcnt lgkmcnt(0)
	v_mfma_f32_32x32x16_f16 v[34:49], v[224:227], v[150:153], v[34:49]
	s_setprio 0
	v_mov_b32_e32 v146, 0
	s_cbranch_vccnz .LBB0_865
	s_mov_b32 s29, 0x41000000
	v_cmp_lg_f32_e64 s[34:35], s1, v194
	v_cmp_lt_f32_e32 vcc, s29, v194
	s_and_b64 s[30:31], s[30:31], s[34:35]
	s_or_b64 s[30:31], vcc, s[30:31]
	v_cndmask_b32_e64 v146, 0, 1, s[30:31]
	v_cmp_ne_u32_e32 vcc, 0, v146
	s_cbranch_vccz .LBB0_864
	v_add_f32_e32 v146, v185, v194
	v_max_f32_e32 v147, v173, v173
	v_max_f32_e32 v173, v147, v146
	v_cmp_neq_f32_e32 vcc, s1, v173
	s_nop 1
	v_cndmask_b32_e32 v146, 0, v173, vcc
	v_sub_f32_e32 v146, v146, v185
	v_exp_f32_e64 v148, -v146
	s_nop 0
	v_pk_mul_f32 v[96:97], v[148:149], v[96:97] op_sel_hi:[0,1]
	v_pk_mul_f32 v[94:95], v[148:149], v[94:95] op_sel_hi:[0,1]
	v_pk_mul_f32 v[92:93], v[148:149], v[92:93] op_sel_hi:[0,1]
	v_pk_mul_f32 v[90:91], v[148:149], v[90:91] op_sel_hi:[0,1]
	v_pk_mul_f32 v[88:89], v[148:149], v[88:89] op_sel_hi:[0,1]
	v_pk_mul_f32 v[86:87], v[148:149], v[86:87] op_sel_hi:[0,1]
	v_pk_mul_f32 v[84:85], v[148:149], v[84:85] op_sel_hi:[0,1]
	v_pk_mul_f32 v[82:83], v[148:149], v[82:83] op_sel_hi:[0,1]
	v_pk_mul_f32 v[80:81], v[148:149], v[80:81] op_sel_hi:[0,1]
	v_pk_mul_f32 v[78:79], v[148:149], v[78:79] op_sel_hi:[0,1]
	v_pk_mul_f32 v[76:77], v[148:149], v[76:77] op_sel_hi:[0,1]
	v_pk_mul_f32 v[74:75], v[148:149], v[74:75] op_sel_hi:[0,1]
	v_pk_mul_f32 v[72:73], v[148:149], v[72:73] op_sel_hi:[0,1]
	v_pk_mul_f32 v[70:71], v[148:149], v[70:71] op_sel_hi:[0,1]
	v_pk_mul_f32 v[68:69], v[148:149], v[68:69] op_sel_hi:[0,1]
	v_pk_mul_f32 v[66:67], v[148:149], v[66:67] op_sel_hi:[0,1]
	v_pk_mul_f32 v[64:65], v[148:149], v[64:65] op_sel_hi:[0,1]
	v_pk_mul_f32 v[62:63], v[148:149], v[62:63] op_sel_hi:[0,1]
	v_pk_mul_f32 v[60:61], v[148:149], v[60:61] op_sel_hi:[0,1]
	v_pk_mul_f32 v[58:59], v[148:149], v[58:59] op_sel_hi:[0,1]
	v_pk_mul_f32 v[56:57], v[148:149], v[56:57] op_sel_hi:[0,1]
	v_pk_mul_f32 v[54:55], v[148:149], v[54:55] op_sel_hi:[0,1]
	v_pk_mul_f32 v[52:53], v[148:149], v[52:53] op_sel_hi:[0,1]
	v_pk_mul_f32 v[50:51], v[148:149], v[50:51] op_sel_hi:[0,1]
	v_pk_mul_f32 v[48:49], v[148:149], v[48:49] op_sel_hi:[0,1]
	v_pk_mul_f32 v[46:47], v[148:149], v[46:47] op_sel_hi:[0,1]
	v_pk_mul_f32 v[44:45], v[148:149], v[44:45] op_sel_hi:[0,1]
	v_pk_mul_f32 v[42:43], v[148:149], v[42:43] op_sel_hi:[0,1]
	v_pk_mul_f32 v[40:41], v[148:149], v[40:41] op_sel_hi:[0,1]
	v_pk_mul_f32 v[38:39], v[148:149], v[38:39] op_sel_hi:[0,1]
	v_pk_mul_f32 v[36:37], v[148:149], v[36:37] op_sel_hi:[0,1]
	v_pk_mul_f32 v[34:35], v[148:149], v[34:35] op_sel_hi:[0,1]
	v_mul_f32_e32 v184, v184, v148
	s_branch .LBB0_865

.LBB0_878:
	s_add_i32 s30, s42, -1
	s_cmp_ge_u32 s30, s90
	s_cbranch_scc1 .LBB0_891
	s_cmp_lt_u32 s42, s90
	v_cmp_eq_f32_e64 s[30:31], s1, v172
	s_cselect_b64 s[40:41], -1, 0
	s_cmp_ge_u32 s42, s90
	v_cndmask_b32_e64 v184, v172, 0, s[30:31]
	s_cbranch_scc1 .LBB0_881
	s_mul_i32 s35, s26, 0x6000
	v_add_u32_e32 v147, s35, v168
	ds_read_b128 v[148:151], v147
	v_xor_b32_e32 v98, 0x80000000, v184
	v_mov_b32_e32 v99, v98
	v_mov_b32_e32 v100, v98
	v_mov_b32_e32 v101, v98
	v_mov_b32_e32 v102, v98
	v_mov_b32_e32 v103, v98
	v_mov_b32_e32 v104, v98
	v_mov_b32_e32 v105, v98
	v_mov_b32_e32 v106, v98
	v_mov_b32_e32 v107, v98
	v_mov_b32_e32 v108, v98
	v_mov_b32_e32 v109, v98
	v_mov_b32_e32 v110, v98
	v_mov_b32_e32 v111, v98
	v_mov_b32_e32 v112, v98
	v_mov_b32_e32 v113, v98
	ds_read_b128 v[152:155], v147 offset:4096
	v_add_u32_e32 v147, s35, v169
	ds_read_b128 v[156:159], v147
	ds_read_b128 v[188:191], v147 offset:4096
	v_add_u32_e32 v147, s35, v170
	ds_read_b128 v[192:195], v147
	ds_read_b128 v[196:199], v147 offset:4096
	v_add_u32_e32 v147, s35, v171
	ds_read_b128 v[208:211], v147
	ds_read_b128 v[212:215], v147 offset:4096
	s_setprio 1
	s_waitcnt lgkmcnt(7)
	s_nop 0
	v_mfma_f32_32x32x16_f16 v[114:129], v[148:151], v[130:133], v[98:113]
	s_waitcnt lgkmcnt(6)
	v_mfma_f32_32x32x16_f16 v[98:113], v[152:155], v[130:133], v[98:113]
	s_waitcnt lgkmcnt(5)
	v_mfma_f32_32x32x16_f16 v[114:129], v[156:159], v[134:137], v[114:129]
	s_waitcnt lgkmcnt(4)
	v_mfma_f32_32x32x16_f16 v[98:113], v[188:191], v[134:137], v[98:113]
	s_waitcnt lgkmcnt(3)
	v_mfma_f32_32x32x16_f16 v[114:129], v[192:195], v[138:141], v[114:129]
	s_waitcnt lgkmcnt(2)
	v_mfma_f32_32x32x16_f16 v[98:113], v[196:199], v[138:141], v[98:113]
	s_waitcnt lgkmcnt(1)
	v_mfma_f32_32x32x16_f16 v[114:129], v[208:211], v[142:145], v[114:129]
	s_waitcnt lgkmcnt(0)
	v_mfma_f32_32x32x16_f16 v[98:113], v[212:215], v[142:145], v[98:113]

.LBB0_887:
	v_exp_f32_e32 v82, v82
	v_exp_f32_e32 v83, v83
	v_exp_f32_e32 v50, v50
	v_exp_f32_e32 v51, v51
	v_exp_f32_e32 v84, v84
	v_exp_f32_e32 v85, v85
	v_exp_f32_e32 v52, v52
	v_exp_f32_e32 v53, v53
	v_exp_f32_e32 v86, v86
	v_exp_f32_e32 v87, v87
	v_exp_f32_e32 v54, v54
	v_exp_f32_e32 v55, v55
	v_exp_f32_e32 v88, v88
	v_exp_f32_e32 v89, v89
	v_exp_f32_e32 v56, v56
	v_exp_f32_e32 v57, v57
	v_pk_add_f32 v[194:195], v[82:83], 0 op_sel_hi:[1,0]
	v_pk_add_f32 v[196:197], v[50:51], 0 op_sel_hi:[1,0]
	v_exp_f32_e32 v90, v90
	v_exp_f32_e32 v91, v91
	v_exp_f32_e32 v58, v58
	v_exp_f32_e32 v59, v59
	v_pk_add_f32 v[194:195], v[84:85], v[194:195]
	v_pk_add_f32 v[196:197], v[52:53], v[196:197]
	v_exp_f32_e32 v92, v92
	v_exp_f32_e32 v93, v93
	v_exp_f32_e32 v60, v60
	v_exp_f32_e32 v61, v61
	v_pk_add_f32 v[194:195], v[86:87], v[194:195]
	v_pk_add_f32 v[196:197], v[54:55], v[196:197]
	v_pk_add_f32 v[194:195], v[88:89], v[194:195]
	v_pk_add_f32 v[196:197], v[56:57], v[196:197]
	v_pk_add_f32 v[194:195], v[90:91], v[194:195]
	v_pk_add_f32 v[196:197], v[58:59], v[196:197]
	v_pk_add_f32 v[208:209], v[92:93], v[194:195]
	v_pk_add_f32 v[210:211], v[60:61], v[196:197]
	v_exp_f32_e32 v94, v94
	v_exp_f32_e32 v95, v95
	v_exp_f32_e32 v62, v62
	v_exp_f32_e32 v63, v63
	v_cvt_pk_f16_f32 v194, v82, v83
	v_cvt_pk_f16_f32 v195, v84, v85
	v_cvt_pk_f16_f32 v196, v86, v87
	v_cvt_pk_f16_f32 v197, v88, v89
	v_exp_f32_e32 v96, v96
	v_exp_f32_e32 v97, v97
	s_waitcnt lgkmcnt(0)
	v_mfma_f32_32x32x16_f16 v[2:17], v[158:161], v[194:197], v[2:17]
	v_exp_f32_e32 v64, v64
	v_exp_f32_e32 v65, v65
	v_pk_add_f32 v[158:159], v[94:95], v[208:209]
	v_pk_add_f32 v[160:161], v[62:63], v[210:211]
	v_pk_add_f32 v[158:159], v[96:97], v[158:159]
	v_pk_add_f32 v[160:161], v[64:65], v[160:161]
	v_mfma_f32_32x32x16_f16 v[18:33], v[154:157], v[194:197], v[18:33]
	v_add_f32_e64 v158, v160, v158
	v_add_f32_e64 v159, v161, v159
	v_cvt_pk_f16_f32 v154, v90, v91
	v_add_f32_e32 v208, v158, v159
	v_add_f32_e32 v183, v183, v208
	v_cvt_pk_f16_f32 v155, v92, v93
	v_cvt_pk_f16_f32 v156, v94, v95
	v_cvt_pk_f16_f32 v157, v96, v97
	v_mfma_f32_32x32x16_f16 v[34:49], v[150:153], v[194:197], v[34:49]
	v_cvt_pk_f16_f32 v158, v50, v51
	v_cvt_pk_f16_f32 v159, v52, v53
	v_cvt_pk_f16_f32 v160, v54, v55
	v_cvt_pk_f16_f32 v161, v56, v57
	v_cvt_pk_f16_f32 v150, v58, v59
	v_cvt_pk_f16_f32 v151, v60, v61
	v_cvt_pk_f16_f32 v152, v62, v63
	v_mfma_f32_32x32x16_f16 v[66:81], v[146:149], v[194:197], v[66:81]
	v_cvt_pk_f16_f32 v153, v64, v65
	s_and_b64 vcc, exec, s[34:35]
	ds_read_b64_tr_b16 v[146:147], v191 offset:12288
	ds_read_b64_tr_b16 v[148:149], v192 offset:12288
	ds_read_b64_tr_b16 v[208:209], v190 offset:12288
	ds_read_b64_tr_b16 v[210:211], v185 offset:12288
	ds_read_b64_tr_b16 v[212:213], v188 offset:12288
	ds_read_b64_tr_b16 v[214:215], v186 offset:12288
	ds_read_b64_tr_b16 v[216:217], v189 offset:12288
	ds_read_b64_tr_b16 v[218:219], v187 offset:12288
	ds_read_b64_tr_b16 v[220:221], v191 offset:16384
	ds_read_b64_tr_b16 v[222:223], v192 offset:16384
	s_waitcnt lgkmcnt(8)
	v_mfma_f32_32x32x16_f16 v[2:17], v[146:149], v[154:157], v[2:17]
	ds_read_b64_tr_b16 v[224:225], v190 offset:16384
	ds_read_b64_tr_b16 v[226:227], v185 offset:16384
	s_waitcnt lgkmcnt(8)
	v_mfma_f32_32x32x16_f16 v[18:33], v[208:211], v[154:157], v[18:33]
	ds_read_b64_tr_b16 v[146:147], v188 offset:16384
	ds_read_b64_tr_b16 v[148:149], v186 offset:16384
	s_waitcnt lgkmcnt(8)
	v_mfma_f32_32x32x16_f16 v[34:49], v[212:215], v[154:157], v[34:49]
	ds_read_b64_tr_b16 v[208:209], v189 offset:16384
	ds_read_b64_tr_b16 v[210:211], v187 offset:16384
	s_waitcnt lgkmcnt(8)
	v_mfma_f32_32x32x16_f16 v[66:81], v[216:219], v[154:157], v[66:81]
	ds_read_b64_tr_b16 v[212:213], v191 offset:20480
	ds_read_b64_tr_b16 v[214:215], v192 offset:20480
	s_waitcnt lgkmcnt(8)
	v_mfma_f32_32x32x16_f16 v[2:17], v[220:223], v[158:161], v[2:17]
	ds_read_b64_tr_b16 v[216:217], v190 offset:20480
	ds_read_b64_tr_b16 v[218:219], v185 offset:20480
	s_waitcnt lgkmcnt(8)
	v_mfma_f32_32x32x16_f16 v[18:33], v[224:227], v[158:161], v[18:33]
	ds_read_b64_tr_b16 v[220:221], v188 offset:20480
	ds_read_b64_tr_b16 v[222:223], v186 offset:20480
	s_waitcnt lgkmcnt(8)
	v_mfma_f32_32x32x16_f16 v[34:49], v[146:149], v[158:161], v[34:49]
	ds_read_b64_tr_b16 v[224:225], v189 offset:20480
	ds_read_b64_tr_b16 v[226:227], v187 offset:20480
	s_waitcnt lgkmcnt(8)
	v_mfma_f32_32x32x16_f16 v[66:81], v[208:211], v[158:161], v[66:81]
	s_waitcnt lgkmcnt(6)
	v_mfma_f32_32x32x16_f16 v[2:17], v[212:215], v[150:153], v[2:17]
	s_waitcnt lgkmcnt(4)
	v_mfma_f32_32x32x16_f16 v[18:33], v[216:219], v[150:153], v[18:33]
	s_waitcnt lgkmcnt(2)
	v_mfma_f32_32x32x16_f16 v[34:49], v[220:223], v[150:153], v[34:49]
	s_waitcnt lgkmcnt(0)
	v_mfma_f32_32x32x16_f16 v[66:81], v[224:227], v[150:153], v[66:81]
	s_setprio 0
	v_mov_b32_e32 v146, 0
	s_cbranch_vccnz .LBB0_891
	s_mov_b32 s28, 0x41000000
	v_cmp_lg_f32_e64 s[34:35], s1, v193
	v_cmp_lt_f32_e32 vcc, s28, v193
	s_and_b64 s[30:31], s[30:31], s[34:35]
	s_or_b64 s[30:31], vcc, s[30:31]
	v_cndmask_b32_e64 v146, 0, 1, s[30:31]
	v_cmp_ne_u32_e32 vcc, 0, v146
	s_cbranch_vccz .LBB0_890
	v_add_f32_e32 v146, v184, v193
	v_max_f32_e32 v147, v172, v172
	v_max_f32_e32 v172, v147, v146
	v_cmp_neq_f32_e32 vcc, s1, v172
	s_nop 1
	v_cndmask_b32_e32 v146, 0, v172, vcc
	v_sub_f32_e32 v146, v146, v184
	v_exp_f32_e64 v148, -v146
	s_nop 0
	v_pk_mul_f32 v[16:17], v[148:149], v[16:17] op_sel_hi:[0,1]
	v_pk_mul_f32 v[14:15], v[148:149], v[14:15] op_sel_hi:[0,1]
	v_pk_mul_f32 v[12:13], v[148:149], v[12:13] op_sel_hi:[0,1]
	v_pk_mul_f32 v[10:11], v[148:149], v[10:11] op_sel_hi:[0,1]
	v_pk_mul_f32 v[8:9], v[148:149], v[8:9] op_sel_hi:[0,1]
	v_pk_mul_f32 v[6:7], v[148:149], v[6:7] op_sel_hi:[0,1]
	v_pk_mul_f32 v[4:5], v[148:149], v[4:5] op_sel_hi:[0,1]
	v_pk_mul_f32 v[2:3], v[148:149], v[2:3] op_sel_hi:[0,1]
	v_pk_mul_f32 v[32:33], v[148:149], v[32:33] op_sel_hi:[0,1]
	v_pk_mul_f32 v[30:31], v[148:149], v[30:31] op_sel_hi:[0,1]
	v_pk_mul_f32 v[28:29], v[148:149], v[28:29] op_sel_hi:[0,1]
	v_pk_mul_f32 v[26:27], v[148:149], v[26:27] op_sel_hi:[0,1]
	v_pk_mul_f32 v[24:25], v[148:149], v[24:25] op_sel_hi:[0,1]
	v_pk_mul_f32 v[22:23], v[148:149], v[22:23] op_sel_hi:[0,1]
	v_pk_mul_f32 v[20:21], v[148:149], v[20:21] op_sel_hi:[0,1]
	v_pk_mul_f32 v[18:19], v[148:149], v[18:19] op_sel_hi:[0,1]
	v_pk_mul_f32 v[48:49], v[148:149], v[48:49] op_sel_hi:[0,1]
	v_pk_mul_f32 v[46:47], v[148:149], v[46:47] op_sel_hi:[0,1]
	v_pk_mul_f32 v[44:45], v[148:149], v[44:45] op_sel_hi:[0,1]
	v_pk_mul_f32 v[42:43], v[148:149], v[42:43] op_sel_hi:[0,1]
	v_pk_mul_f32 v[40:41], v[148:149], v[40:41] op_sel_hi:[0,1]
	v_pk_mul_f32 v[38:39], v[148:149], v[38:39] op_sel_hi:[0,1]
	v_pk_mul_f32 v[36:37], v[148:149], v[36:37] op_sel_hi:[0,1]
	v_pk_mul_f32 v[34:35], v[148:149], v[34:35] op_sel_hi:[0,1]
	v_pk_mul_f32 v[80:81], v[148:149], v[80:81] op_sel_hi:[0,1]
	v_pk_mul_f32 v[78:79], v[148:149], v[78:79] op_sel_hi:[0,1]
	v_pk_mul_f32 v[76:77], v[148:149], v[76:77] op_sel_hi:[0,1]
	v_pk_mul_f32 v[74:75], v[148:149], v[74:75] op_sel_hi:[0,1]
	v_pk_mul_f32 v[72:73], v[148:149], v[72:73] op_sel_hi:[0,1]
	v_pk_mul_f32 v[70:71], v[148:149], v[70:71] op_sel_hi:[0,1]
	v_pk_mul_f32 v[68:69], v[148:149], v[68:69] op_sel_hi:[0,1]
	v_pk_mul_f32 v[66:67], v[148:149], v[66:67] op_sel_hi:[0,1]
	v_mul_f32_e32 v183, v183, v148
	s_branch .LBB0_891

.LBB0_896:
	s_cmp_ge_u32 s42, s90
	s_cbranch_scc1 .LBB0_910
	s_cmp_lt_u32 s44, s90
	v_cmp_eq_f32_e64 s[30:31], s1, v172
	s_cselect_b64 s[40:41], -1, 0
	s_cmp_ge_u32 s44, s90
	v_cndmask_b32_e64 v184, v172, 0, s[30:31]
	s_cbranch_scc1 .LBB0_899
	s_mul_i32 s34, s45, 0x6000
	v_add_u32_e32 v147, s34, v168
	ds_read_b128 v[148:151], v147
	v_xor_b32_e32 v50, 0x80000000, v184
	v_mov_b32_e32 v51, v50
	v_mov_b32_e32 v52, v50
	v_mov_b32_e32 v53, v50
	v_mov_b32_e32 v54, v50
	v_mov_b32_e32 v55, v50
	v_mov_b32_e32 v56, v50
	v_mov_b32_e32 v57, v50
	v_mov_b32_e32 v58, v50
	v_mov_b32_e32 v59, v50
	v_mov_b32_e32 v60, v50
	v_mov_b32_e32 v61, v50
	v_mov_b32_e32 v62, v50
	v_mov_b32_e32 v63, v50
	v_mov_b32_e32 v64, v50
	v_mov_b32_e32 v65, v50
	ds_read_b128 v[152:155], v147 offset:4096
	v_add_u32_e32 v147, s34, v169
	ds_read_b128 v[156:159], v147
	ds_read_b128 v[188:191], v147 offset:4096
	v_add_u32_e32 v147, s34, v170
	ds_read_b128 v[192:195], v147
	ds_read_b128 v[196:199], v147 offset:4096
	v_add_u32_e32 v147, s34, v171
	ds_read_b128 v[208:211], v147
	ds_read_b128 v[212:215], v147 offset:4096
	s_setprio 1
	s_waitcnt lgkmcnt(7)
	s_nop 0
	v_mfma_f32_32x32x16_f16 v[82:97], v[148:151], v[130:133], v[50:65]
	s_waitcnt lgkmcnt(6)
	v_mfma_f32_32x32x16_f16 v[50:65], v[152:155], v[130:133], v[50:65]
	s_waitcnt lgkmcnt(5)
	v_mfma_f32_32x32x16_f16 v[82:97], v[156:159], v[134:137], v[82:97]
	s_waitcnt lgkmcnt(4)
	v_mfma_f32_32x32x16_f16 v[50:65], v[188:191], v[134:137], v[50:65]
	s_waitcnt lgkmcnt(3)
	v_mfma_f32_32x32x16_f16 v[82:97], v[192:195], v[138:141], v[82:97]
	s_waitcnt lgkmcnt(2)
	v_mfma_f32_32x32x16_f16 v[50:65], v[196:199], v[138:141], v[50:65]
	s_waitcnt lgkmcnt(1)
	v_mfma_f32_32x32x16_f16 v[82:97], v[208:211], v[142:145], v[82:97]
	s_waitcnt lgkmcnt(0)
	v_mfma_f32_32x32x16_f16 v[50:65], v[212:215], v[142:145], v[50:65]

.LBB0_905:
	v_exp_f32_e32 v114, v114
	v_exp_f32_e32 v115, v115
	v_exp_f32_e32 v98, v98
	v_exp_f32_e32 v99, v99
	v_exp_f32_e32 v116, v116
	v_exp_f32_e32 v117, v117
	v_exp_f32_e32 v100, v100
	v_exp_f32_e32 v101, v101
	v_exp_f32_e32 v118, v118
	v_exp_f32_e32 v119, v119
	v_exp_f32_e32 v102, v102
	v_exp_f32_e32 v103, v103
	v_exp_f32_e32 v120, v120
	v_exp_f32_e32 v121, v121
	v_exp_f32_e32 v104, v104
	v_exp_f32_e32 v105, v105
	v_pk_add_f32 v[194:195], v[114:115], 0 op_sel_hi:[1,0]
	v_pk_add_f32 v[196:197], v[98:99], 0 op_sel_hi:[1,0]
	v_exp_f32_e32 v122, v122
	v_exp_f32_e32 v123, v123
	v_exp_f32_e32 v106, v106
	v_exp_f32_e32 v107, v107
	v_pk_add_f32 v[194:195], v[116:117], v[194:195]
	v_pk_add_f32 v[196:197], v[100:101], v[196:197]
	v_exp_f32_e32 v124, v124
	v_exp_f32_e32 v125, v125
	v_exp_f32_e32 v108, v108
	v_exp_f32_e32 v109, v109
	v_pk_add_f32 v[194:195], v[118:119], v[194:195]
	v_pk_add_f32 v[196:197], v[102:103], v[196:197]
	v_pk_add_f32 v[194:195], v[120:121], v[194:195]
	v_pk_add_f32 v[196:197], v[104:105], v[196:197]
	v_pk_add_f32 v[194:195], v[122:123], v[194:195]
	v_pk_add_f32 v[196:197], v[106:107], v[196:197]
	v_pk_add_f32 v[208:209], v[124:125], v[194:195]
	v_pk_add_f32 v[210:211], v[108:109], v[196:197]
	v_exp_f32_e32 v126, v126
	v_exp_f32_e32 v127, v127
	v_exp_f32_e32 v110, v110
	v_exp_f32_e32 v111, v111
	v_cvt_pk_f16_f32 v194, v114, v115
	v_cvt_pk_f16_f32 v195, v116, v117
	v_cvt_pk_f16_f32 v196, v118, v119
	v_cvt_pk_f16_f32 v197, v120, v121
	v_exp_f32_e32 v128, v128
	v_exp_f32_e32 v129, v129
	s_waitcnt lgkmcnt(0)
	v_mfma_f32_32x32x16_f16 v[2:17], v[158:161], v[194:197], v[2:17]
	v_exp_f32_e32 v112, v112
	v_exp_f32_e32 v113, v113
	v_pk_add_f32 v[158:159], v[126:127], v[208:209]
	v_pk_add_f32 v[160:161], v[110:111], v[210:211]
	v_pk_add_f32 v[158:159], v[128:129], v[158:159]
	v_pk_add_f32 v[160:161], v[112:113], v[160:161]
	v_mfma_f32_32x32x16_f16 v[18:33], v[154:157], v[194:197], v[18:33]
	v_add_f32_e64 v158, v158, v160
	v_add_f32_e64 v159, v159, v161
	v_cvt_pk_f16_f32 v154, v122, v123
	v_add_f32_e32 v208, v158, v159
	v_add_f32_e32 v183, v183, v208
	v_cvt_pk_f16_f32 v155, v124, v125
	v_cvt_pk_f16_f32 v156, v126, v127
	v_cvt_pk_f16_f32 v157, v128, v129
	v_mfma_f32_32x32x16_f16 v[34:49], v[150:153], v[194:197], v[34:49]
	v_cvt_pk_f16_f32 v158, v98, v99
	v_cvt_pk_f16_f32 v159, v100, v101
	v_cvt_pk_f16_f32 v160, v102, v103
	v_cvt_pk_f16_f32 v161, v104, v105
	v_cvt_pk_f16_f32 v150, v106, v107
	v_cvt_pk_f16_f32 v151, v108, v109
	v_cvt_pk_f16_f32 v152, v110, v111
	v_mfma_f32_32x32x16_f16 v[66:81], v[146:149], v[194:197], v[66:81]
	v_cvt_pk_f16_f32 v153, v112, v113
	s_and_b64 vcc, exec, s[34:35]
	ds_read_b64_tr_b16 v[146:147], v191 offset:12288
	ds_read_b64_tr_b16 v[148:149], v192 offset:12288
	ds_read_b64_tr_b16 v[208:209], v190 offset:12288
	ds_read_b64_tr_b16 v[210:211], v185 offset:12288
	ds_read_b64_tr_b16 v[212:213], v188 offset:12288
	ds_read_b64_tr_b16 v[214:215], v186 offset:12288
	ds_read_b64_tr_b16 v[216:217], v189 offset:12288
	ds_read_b64_tr_b16 v[218:219], v187 offset:12288
	ds_read_b64_tr_b16 v[220:221], v191 offset:16384
	ds_read_b64_tr_b16 v[222:223], v192 offset:16384
	s_waitcnt lgkmcnt(8)
	v_mfma_f32_32x32x16_f16 v[2:17], v[146:149], v[154:157], v[2:17]
	ds_read_b64_tr_b16 v[224:225], v190 offset:16384
	ds_read_b64_tr_b16 v[226:227], v185 offset:16384
	s_waitcnt lgkmcnt(8)
	v_mfma_f32_32x32x16_f16 v[18:33], v[208:211], v[154:157], v[18:33]
	ds_read_b64_tr_b16 v[146:147], v188 offset:16384
	ds_read_b64_tr_b16 v[148:149], v186 offset:16384
	s_waitcnt lgkmcnt(8)
	v_mfma_f32_32x32x16_f16 v[34:49], v[212:215], v[154:157], v[34:49]
	ds_read_b64_tr_b16 v[208:209], v189 offset:16384
	ds_read_b64_tr_b16 v[210:211], v187 offset:16384
	s_waitcnt lgkmcnt(8)
	v_mfma_f32_32x32x16_f16 v[66:81], v[216:219], v[154:157], v[66:81]
	ds_read_b64_tr_b16 v[212:213], v191 offset:20480
	ds_read_b64_tr_b16 v[214:215], v192 offset:20480
	s_waitcnt lgkmcnt(8)
	v_mfma_f32_32x32x16_f16 v[2:17], v[220:223], v[158:161], v[2:17]
	ds_read_b64_tr_b16 v[216:217], v190 offset:20480
	ds_read_b64_tr_b16 v[218:219], v185 offset:20480
	s_waitcnt lgkmcnt(8)
	v_mfma_f32_32x32x16_f16 v[18:33], v[224:227], v[158:161], v[18:33]
	ds_read_b64_tr_b16 v[220:221], v188 offset:20480
	ds_read_b64_tr_b16 v[222:223], v186 offset:20480
	s_waitcnt lgkmcnt(8)
	v_mfma_f32_32x32x16_f16 v[34:49], v[146:149], v[158:161], v[34:49]
	ds_read_b64_tr_b16 v[224:225], v189 offset:20480
	ds_read_b64_tr_b16 v[226:227], v187 offset:20480
	s_waitcnt lgkmcnt(8)
	v_mfma_f32_32x32x16_f16 v[66:81], v[208:211], v[158:161], v[66:81]
	s_waitcnt lgkmcnt(6)
	v_mfma_f32_32x32x16_f16 v[2:17], v[212:215], v[150:153], v[2:17]
	s_waitcnt lgkmcnt(4)
	v_mfma_f32_32x32x16_f16 v[18:33], v[216:219], v[150:153], v[18:33]
	s_waitcnt lgkmcnt(2)
	v_mfma_f32_32x32x16_f16 v[34:49], v[220:223], v[150:153], v[34:49]
	s_waitcnt lgkmcnt(0)
	v_mfma_f32_32x32x16_f16 v[66:81], v[224:227], v[150:153], v[66:81]
	s_setprio 0
	v_mov_b32_e32 v146, 0
	s_cbranch_vccnz .LBB0_910
	s_mov_b32 s26, 0x41000000
	v_cmp_lg_f32_e64 s[34:35], s1, v193
	v_cmp_lt_f32_e32 vcc, s26, v193
	s_and_b64 s[30:31], s[30:31], s[34:35]
	s_or_b64 s[30:31], vcc, s[30:31]
	v_cndmask_b32_e64 v146, 0, 1, s[30:31]
	v_cmp_ne_u32_e32 vcc, 0, v146
	s_cbranch_vccz .LBB0_909
	v_add_f32_e32 v146, v184, v193
	v_max_f32_e32 v147, v172, v172
	v_max_f32_e32 v172, v147, v146
	v_cmp_neq_f32_e32 vcc, s1, v172
	s_nop 1
	v_cndmask_b32_e32 v146, 0, v172, vcc
	v_sub_f32_e32 v146, v146, v184
	v_exp_f32_e64 v148, -v146
	s_nop 0
	v_pk_mul_f32 v[16:17], v[148:149], v[16:17] op_sel_hi:[0,1]
	v_pk_mul_f32 v[14:15], v[148:149], v[14:15] op_sel_hi:[0,1]
	v_pk_mul_f32 v[12:13], v[148:149], v[12:13] op_sel_hi:[0,1]
	v_pk_mul_f32 v[10:11], v[148:149], v[10:11] op_sel_hi:[0,1]
	v_pk_mul_f32 v[8:9], v[148:149], v[8:9] op_sel_hi:[0,1]
	v_pk_mul_f32 v[6:7], v[148:149], v[6:7] op_sel_hi:[0,1]
	v_pk_mul_f32 v[4:5], v[148:149], v[4:5] op_sel_hi:[0,1]
	v_pk_mul_f32 v[2:3], v[148:149], v[2:3] op_sel_hi:[0,1]
	v_pk_mul_f32 v[32:33], v[148:149], v[32:33] op_sel_hi:[0,1]
	v_pk_mul_f32 v[30:31], v[148:149], v[30:31] op_sel_hi:[0,1]
	v_pk_mul_f32 v[28:29], v[148:149], v[28:29] op_sel_hi:[0,1]
	v_pk_mul_f32 v[26:27], v[148:149], v[26:27] op_sel_hi:[0,1]
	v_pk_mul_f32 v[24:25], v[148:149], v[24:25] op_sel_hi:[0,1]
	v_pk_mul_f32 v[22:23], v[148:149], v[22:23] op_sel_hi:[0,1]
	v_pk_mul_f32 v[20:21], v[148:149], v[20:21] op_sel_hi:[0,1]
	v_pk_mul_f32 v[18:19], v[148:149], v[18:19] op_sel_hi:[0,1]
	v_pk_mul_f32 v[48:49], v[148:149], v[48:49] op_sel_hi:[0,1]
	v_pk_mul_f32 v[46:47], v[148:149], v[46:47] op_sel_hi:[0,1]
	v_pk_mul_f32 v[44:45], v[148:149], v[44:45] op_sel_hi:[0,1]
	v_pk_mul_f32 v[42:43], v[148:149], v[42:43] op_sel_hi:[0,1]
	v_pk_mul_f32 v[40:41], v[148:149], v[40:41] op_sel_hi:[0,1]
	v_pk_mul_f32 v[38:39], v[148:149], v[38:39] op_sel_hi:[0,1]
	v_pk_mul_f32 v[36:37], v[148:149], v[36:37] op_sel_hi:[0,1]
	v_pk_mul_f32 v[34:35], v[148:149], v[34:35] op_sel_hi:[0,1]
	v_pk_mul_f32 v[80:81], v[148:149], v[80:81] op_sel_hi:[0,1]
	v_pk_mul_f32 v[78:79], v[148:149], v[78:79] op_sel_hi:[0,1]
	v_pk_mul_f32 v[76:77], v[148:149], v[76:77] op_sel_hi:[0,1]
	v_pk_mul_f32 v[74:75], v[148:149], v[74:75] op_sel_hi:[0,1]
	v_pk_mul_f32 v[72:73], v[148:149], v[72:73] op_sel_hi:[0,1]
	v_pk_mul_f32 v[70:71], v[148:149], v[70:71] op_sel_hi:[0,1]
	v_pk_mul_f32 v[68:69], v[148:149], v[68:69] op_sel_hi:[0,1]
	v_pk_mul_f32 v[66:67], v[148:149], v[66:67] op_sel_hi:[0,1]
	v_mul_f32_e32 v183, v183, v148
	s_branch .LBB0_910
